# speedup vs baseline: 1.0232x; 1.0119x over previous
_Z5k_mixPKhPKfPhi:
	s_load_dwordx4 s[4:7], s[0:1], 0x0
	s_load_dwordx2 s[8:9], s[0:1], 0x10
	s_load_dword s10, s[0:1], 0x18
	v_lshl_or_b32 v1, s2, 8, v0
	v_lshlrev_b32_e32 v2, 4, v1
	v_lshrrev_b32_e32 v3, 5, v1
	s_mov_b32 s28, 0x41800000
	s_mov_b32 s30, 0x41000000
	s_waitcnt lgkmcnt(0)
	v_add_u32_e32 v3, s10, v3
	v_lshlrev_b32_e32 v3, 5, v3
	s_add_u32 s26, s6, 0x80000
	s_addc_u32 s27, s7, 0
	s_add_u32 s12, s4, 0x800000
	s_addc_u32 s13, s5, 0
	s_add_u32 s14, s12, 0x800000
	s_addc_u32 s15, s13, 0
	s_add_u32 s16, s14, 0x800000
	s_addc_u32 s17, s15, 0
	s_add_u32 s18, s16, 0x800000
	s_addc_u32 s19, s17, 0
	s_add_u32 s20, s18, 0x800000
	s_addc_u32 s21, s19, 0
	s_add_u32 s22, s20, 0x800000
	s_addc_u32 s23, s21, 0
	s_add_u32 s24, s22, 0x800000
	s_addc_u32 s25, s23, 0
	s_add_u32 s32, s8, 0x800000
	s_addc_u32 s33, s9, 0
	global_load_dwordx4 v[100:103], v3, s[6:7]
	global_load_dwordx4 v[104:107], v3, s[6:7] offset:16
	global_load_dwordx4 v[108:111], v3, s[26:27]
	global_load_dwordx4 v[112:115], v3, s[26:27] offset:16
	global_load_dwordx4 v[68:71], v2, s[4:5]
	global_load_dwordx4 v[72:75], v2, s[12:13]
	global_load_dwordx4 v[76:79], v2, s[14:15]
	global_load_dwordx4 v[80:83], v2, s[16:17]
	global_load_dwordx4 v[84:87], v2, s[18:19]
	global_load_dwordx4 v[88:91], v2, s[20:21]
	global_load_dwordx4 v[92:95], v2, s[22:23]
	global_load_dwordx4 v[96:99], v2, s[24:25]
	v_lshl_add_u32 v1, s10, 9, v2
	s_waitcnt vmcnt(8)
	v_pk_mul_f32 v[100:101], v[100:101], s[28:29] op_sel_hi:[1,0]
	v_pk_mul_f32 v[102:103], v[102:103], s[28:29] op_sel_hi:[1,0]
	v_pk_mul_f32 v[104:105], v[104:105], s[28:29] op_sel_hi:[1,0]
	v_pk_mul_f32 v[106:107], v[106:107], s[28:29] op_sel_hi:[1,0]
	v_pk_mul_f32 v[108:109], v[108:109], s[28:29] op_sel_hi:[1,0]
	v_pk_mul_f32 v[110:111], v[110:111], s[28:29] op_sel_hi:[1,0]
	v_pk_mul_f32 v[112:113], v[112:113], s[28:29] op_sel_hi:[1,0]
	v_pk_mul_f32 v[114:115], v[114:115], s[28:29] op_sel_hi:[1,0]
	s_waitcnt vmcnt(7)
	v_cvt_scalef32_pk_f32_fp4 v[116:117], v68, 1.0
	v_cvt_scalef32_pk_f32_fp4 v[118:119], v68, 1.0 op_sel:[1,0,0]
	v_cvt_scalef32_pk_f32_fp4 v[120:121], v68, 1.0 op_sel:[0,1,0]
	v_cvt_scalef32_pk_f32_fp4 v[122:123], v68, 1.0 op_sel:[1,1,0]
	v_pk_mul_f32 v[4:5], v[116:117], v[100:101] op_sel_hi:[1,0]
	v_pk_mul_f32 v[36:37], v[116:117], v[108:109] op_sel_hi:[1,0]
	v_pk_mul_f32 v[6:7], v[118:119], v[100:101] op_sel_hi:[1,0]
	v_pk_mul_f32 v[38:39], v[118:119], v[108:109] op_sel_hi:[1,0]
	v_pk_mul_f32 v[8:9], v[120:121], v[100:101] op_sel_hi:[1,0]
	v_pk_mul_f32 v[40:41], v[120:121], v[108:109] op_sel_hi:[1,0]
	v_pk_mul_f32 v[10:11], v[122:123], v[100:101] op_sel_hi:[1,0]
	v_pk_mul_f32 v[42:43], v[122:123], v[108:109] op_sel_hi:[1,0]
	v_cvt_scalef32_pk_f32_fp4 v[116:117], v69, 1.0
	v_cvt_scalef32_pk_f32_fp4 v[118:119], v69, 1.0 op_sel:[1,0,0]
	v_cvt_scalef32_pk_f32_fp4 v[120:121], v69, 1.0 op_sel:[0,1,0]
	v_cvt_scalef32_pk_f32_fp4 v[122:123], v69, 1.0 op_sel:[1,1,0]
	v_pk_mul_f32 v[12:13], v[116:117], v[100:101] op_sel_hi:[1,0]
	v_pk_mul_f32 v[44:45], v[116:117], v[108:109] op_sel_hi:[1,0]
	v_pk_mul_f32 v[14:15], v[118:119], v[100:101] op_sel_hi:[1,0]
	v_pk_mul_f32 v[46:47], v[118:119], v[108:109] op_sel_hi:[1,0]
	v_pk_mul_f32 v[16:17], v[120:121], v[100:101] op_sel_hi:[1,0]
	v_pk_mul_f32 v[48:49], v[120:121], v[108:109] op_sel_hi:[1,0]
	v_pk_mul_f32 v[18:19], v[122:123], v[100:101] op_sel_hi:[1,0]
	v_pk_mul_f32 v[50:51], v[122:123], v[108:109] op_sel_hi:[1,0]
	v_cvt_scalef32_pk_f32_fp4 v[116:117], v70, 1.0
	v_cvt_scalef32_pk_f32_fp4 v[118:119], v70, 1.0 op_sel:[1,0,0]
	v_cvt_scalef32_pk_f32_fp4 v[120:121], v70, 1.0 op_sel:[0,1,0]
	v_cvt_scalef32_pk_f32_fp4 v[122:123], v70, 1.0 op_sel:[1,1,0]
	v_pk_mul_f32 v[20:21], v[116:117], v[100:101] op_sel_hi:[1,0]
	v_pk_mul_f32 v[52:53], v[116:117], v[108:109] op_sel_hi:[1,0]
	v_pk_mul_f32 v[22:23], v[118:119], v[100:101] op_sel_hi:[1,0]
	v_pk_mul_f32 v[54:55], v[118:119], v[108:109] op_sel_hi:[1,0]
	v_pk_mul_f32 v[24:25], v[120:121], v[100:101] op_sel_hi:[1,0]
	v_pk_mul_f32 v[56:57], v[120:121], v[108:109] op_sel_hi:[1,0]
	v_pk_mul_f32 v[26:27], v[122:123], v[100:101] op_sel_hi:[1,0]
	v_pk_mul_f32 v[58:59], v[122:123], v[108:109] op_sel_hi:[1,0]
	v_cvt_scalef32_pk_f32_fp4 v[116:117], v71, 1.0
	v_cvt_scalef32_pk_f32_fp4 v[118:119], v71, 1.0 op_sel:[1,0,0]
	v_cvt_scalef32_pk_f32_fp4 v[120:121], v71, 1.0 op_sel:[0,1,0]
	v_cvt_scalef32_pk_f32_fp4 v[122:123], v71, 1.0 op_sel:[1,1,0]
	v_pk_mul_f32 v[28:29], v[116:117], v[100:101] op_sel_hi:[1,0]
	v_pk_mul_f32 v[60:61], v[116:117], v[108:109] op_sel_hi:[1,0]
	v_pk_mul_f32 v[30:31], v[118:119], v[100:101] op_sel_hi:[1,0]
	v_pk_mul_f32 v[62:63], v[118:119], v[108:109] op_sel_hi:[1,0]
	v_pk_mul_f32 v[32:33], v[120:121], v[100:101] op_sel_hi:[1,0]
	v_pk_mul_f32 v[64:65], v[120:121], v[108:109] op_sel_hi:[1,0]
	v_pk_mul_f32 v[34:35], v[122:123], v[100:101] op_sel_hi:[1,0]
	v_pk_mul_f32 v[66:67], v[122:123], v[108:109] op_sel_hi:[1,0]
	s_waitcnt vmcnt(6)
	v_cvt_scalef32_pk_f32_fp4 v[116:117], v72, 1.0
	v_cvt_scalef32_pk_f32_fp4 v[118:119], v72, 1.0 op_sel:[1,0,0]
	v_cvt_scalef32_pk_f32_fp4 v[120:121], v72, 1.0 op_sel:[0,1,0]
	v_cvt_scalef32_pk_f32_fp4 v[122:123], v72, 1.0 op_sel:[1,1,0]
	v_pk_fma_f32 v[4:5], v[116:117], v[100:101], v[4:5] op_sel:[0,1,0] op_sel_hi:[1,1,1]
	v_pk_fma_f32 v[36:37], v[116:117], v[108:109], v[36:37] op_sel:[0,1,0] op_sel_hi:[1,1,1]
	v_pk_fma_f32 v[6:7], v[118:119], v[100:101], v[6:7] op_sel:[0,1,0] op_sel_hi:[1,1,1]
	v_pk_fma_f32 v[38:39], v[118:119], v[108:109], v[38:39] op_sel:[0,1,0] op_sel_hi:[1,1,1]
	v_pk_fma_f32 v[8:9], v[120:121], v[100:101], v[8:9] op_sel:[0,1,0] op_sel_hi:[1,1,1]
	v_pk_fma_f32 v[40:41], v[120:121], v[108:109], v[40:41] op_sel:[0,1,0] op_sel_hi:[1,1,1]
	v_pk_fma_f32 v[10:11], v[122:123], v[100:101], v[10:11] op_sel:[0,1,0] op_sel_hi:[1,1,1]
	v_pk_fma_f32 v[42:43], v[122:123], v[108:109], v[42:43] op_sel:[0,1,0] op_sel_hi:[1,1,1]
	v_cvt_scalef32_pk_f32_fp4 v[116:117], v73, 1.0
	v_cvt_scalef32_pk_f32_fp4 v[118:119], v73, 1.0 op_sel:[1,0,0]
	v_cvt_scalef32_pk_f32_fp4 v[120:121], v73, 1.0 op_sel:[0,1,0]
	v_cvt_scalef32_pk_f32_fp4 v[122:123], v73, 1.0 op_sel:[1,1,0]
	v_pk_fma_f32 v[12:13], v[116:117], v[100:101], v[12:13] op_sel:[0,1,0] op_sel_hi:[1,1,1]
	v_pk_fma_f32 v[44:45], v[116:117], v[108:109], v[44:45] op_sel:[0,1,0] op_sel_hi:[1,1,1]
	v_pk_fma_f32 v[14:15], v[118:119], v[100:101], v[14:15] op_sel:[0,1,0] op_sel_hi:[1,1,1]
	v_pk_fma_f32 v[46:47], v[118:119], v[108:109], v[46:47] op_sel:[0,1,0] op_sel_hi:[1,1,1]
	v_pk_fma_f32 v[16:17], v[120:121], v[100:101], v[16:17] op_sel:[0,1,0] op_sel_hi:[1,1,1]
	v_pk_fma_f32 v[48:49], v[120:121], v[108:109], v[48:49] op_sel:[0,1,0] op_sel_hi:[1,1,1]
	v_pk_fma_f32 v[18:19], v[122:123], v[100:101], v[18:19] op_sel:[0,1,0] op_sel_hi:[1,1,1]
	v_pk_fma_f32 v[50:51], v[122:123], v[108:109], v[50:51] op_sel:[0,1,0] op_sel_hi:[1,1,1]
	v_cvt_scalef32_pk_f32_fp4 v[116:117], v74, 1.0
	v_cvt_scalef32_pk_f32_fp4 v[118:119], v74, 1.0 op_sel:[1,0,0]
	v_cvt_scalef32_pk_f32_fp4 v[120:121], v74, 1.0 op_sel:[0,1,0]
	v_cvt_scalef32_pk_f32_fp4 v[122:123], v74, 1.0 op_sel:[1,1,0]
	v_pk_fma_f32 v[20:21], v[116:117], v[100:101], v[20:21] op_sel:[0,1,0] op_sel_hi:[1,1,1]
	v_pk_fma_f32 v[52:53], v[116:117], v[108:109], v[52:53] op_sel:[0,1,0] op_sel_hi:[1,1,1]
	v_pk_fma_f32 v[22:23], v[118:119], v[100:101], v[22:23] op_sel:[0,1,0] op_sel_hi:[1,1,1]
	v_pk_fma_f32 v[54:55], v[118:119], v[108:109], v[54:55] op_sel:[0,1,0] op_sel_hi:[1,1,1]
	v_pk_fma_f32 v[24:25], v[120:121], v[100:101], v[24:25] op_sel:[0,1,0] op_sel_hi:[1,1,1]
	v_pk_fma_f32 v[56:57], v[120:121], v[108:109], v[56:57] op_sel:[0,1,0] op_sel_hi:[1,1,1]
	v_pk_fma_f32 v[26:27], v[122:123], v[100:101], v[26:27] op_sel:[0,1,0] op_sel_hi:[1,1,1]
	v_pk_fma_f32 v[58:59], v[122:123], v[108:109], v[58:59] op_sel:[0,1,0] op_sel_hi:[1,1,1]
	v_cvt_scalef32_pk_f32_fp4 v[116:117], v75, 1.0
	v_cvt_scalef32_pk_f32_fp4 v[118:119], v75, 1.0 op_sel:[1,0,0]
	v_cvt_scalef32_pk_f32_fp4 v[120:121], v75, 1.0 op_sel:[0,1,0]
	v_cvt_scalef32_pk_f32_fp4 v[122:123], v75, 1.0 op_sel:[1,1,0]
	v_pk_fma_f32 v[28:29], v[116:117], v[100:101], v[28:29] op_sel:[0,1,0] op_sel_hi:[1,1,1]
	v_pk_fma_f32 v[60:61], v[116:117], v[108:109], v[60:61] op_sel:[0,1,0] op_sel_hi:[1,1,1]
	v_pk_fma_f32 v[30:31], v[118:119], v[100:101], v[30:31] op_sel:[0,1,0] op_sel_hi:[1,1,1]
	v_pk_fma_f32 v[62:63], v[118:119], v[108:109], v[62:63] op_sel:[0,1,0] op_sel_hi:[1,1,1]
	v_pk_fma_f32 v[32:33], v[120:121], v[100:101], v[32:33] op_sel:[0,1,0] op_sel_hi:[1,1,1]
	v_pk_fma_f32 v[64:65], v[120:121], v[108:109], v[64:65] op_sel:[0,1,0] op_sel_hi:[1,1,1]
	v_pk_fma_f32 v[34:35], v[122:123], v[100:101], v[34:35] op_sel:[0,1,0] op_sel_hi:[1,1,1]
	v_pk_fma_f32 v[66:67], v[122:123], v[108:109], v[66:67] op_sel:[0,1,0] op_sel_hi:[1,1,1]
	s_waitcnt vmcnt(5)
	v_cvt_scalef32_pk_f32_fp4 v[116:117], v76, 1.0
	v_cvt_scalef32_pk_f32_fp4 v[118:119], v76, 1.0 op_sel:[1,0,0]
	v_cvt_scalef32_pk_f32_fp4 v[120:121], v76, 1.0 op_sel:[0,1,0]
	v_cvt_scalef32_pk_f32_fp4 v[122:123], v76, 1.0 op_sel:[1,1,0]
	v_pk_fma_f32 v[4:5], v[116:117], v[102:103], v[4:5] op_sel_hi:[1,0,1]
	v_pk_fma_f32 v[36:37], v[116:117], v[110:111], v[36:37] op_sel_hi:[1,0,1]
	v_pk_fma_f32 v[6:7], v[118:119], v[102:103], v[6:7] op_sel_hi:[1,0,1]
	v_pk_fma_f32 v[38:39], v[118:119], v[110:111], v[38:39] op_sel_hi:[1,0,1]
	v_pk_fma_f32 v[8:9], v[120:121], v[102:103], v[8:9] op_sel_hi:[1,0,1]
	v_pk_fma_f32 v[40:41], v[120:121], v[110:111], v[40:41] op_sel_hi:[1,0,1]
	v_pk_fma_f32 v[10:11], v[122:123], v[102:103], v[10:11] op_sel_hi:[1,0,1]
	v_pk_fma_f32 v[42:43], v[122:123], v[110:111], v[42:43] op_sel_hi:[1,0,1]
	v_cvt_scalef32_pk_f32_fp4 v[116:117], v77, 1.0
	v_cvt_scalef32_pk_f32_fp4 v[118:119], v77, 1.0 op_sel:[1,0,0]
	v_cvt_scalef32_pk_f32_fp4 v[120:121], v77, 1.0 op_sel:[0,1,0]
	v_cvt_scalef32_pk_f32_fp4 v[122:123], v77, 1.0 op_sel:[1,1,0]
	v_pk_fma_f32 v[12:13], v[116:117], v[102:103], v[12:13] op_sel_hi:[1,0,1]
	v_pk_fma_f32 v[44:45], v[116:117], v[110:111], v[44:45] op_sel_hi:[1,0,1]
	v_pk_fma_f32 v[14:15], v[118:119], v[102:103], v[14:15] op_sel_hi:[1,0,1]
	v_pk_fma_f32 v[46:47], v[118:119], v[110:111], v[46:47] op_sel_hi:[1,0,1]
	v_pk_fma_f32 v[16:17], v[120:121], v[102:103], v[16:17] op_sel_hi:[1,0,1]
	v_pk_fma_f32 v[48:49], v[120:121], v[110:111], v[48:49] op_sel_hi:[1,0,1]
	v_pk_fma_f32 v[18:19], v[122:123], v[102:103], v[18:19] op_sel_hi:[1,0,1]
	v_pk_fma_f32 v[50:51], v[122:123], v[110:111], v[50:51] op_sel_hi:[1,0,1]
	v_cvt_scalef32_pk_f32_fp4 v[116:117], v78, 1.0
	v_cvt_scalef32_pk_f32_fp4 v[118:119], v78, 1.0 op_sel:[1,0,0]
	v_cvt_scalef32_pk_f32_fp4 v[120:121], v78, 1.0 op_sel:[0,1,0]
	v_cvt_scalef32_pk_f32_fp4 v[122:123], v78, 1.0 op_sel:[1,1,0]
	v_pk_fma_f32 v[20:21], v[116:117], v[102:103], v[20:21] op_sel_hi:[1,0,1]
	v_pk_fma_f32 v[52:53], v[116:117], v[110:111], v[52:53] op_sel_hi:[1,0,1]
	v_pk_fma_f32 v[22:23], v[118:119], v[102:103], v[22:23] op_sel_hi:[1,0,1]
	v_pk_fma_f32 v[54:55], v[118:119], v[110:111], v[54:55] op_sel_hi:[1,0,1]
	v_pk_fma_f32 v[24:25], v[120:121], v[102:103], v[24:25] op_sel_hi:[1,0,1]
	v_pk_fma_f32 v[56:57], v[120:121], v[110:111], v[56:57] op_sel_hi:[1,0,1]
	v_pk_fma_f32 v[26:27], v[122:123], v[102:103], v[26:27] op_sel_hi:[1,0,1]
	v_pk_fma_f32 v[58:59], v[122:123], v[110:111], v[58:59] op_sel_hi:[1,0,1]
	v_cvt_scalef32_pk_f32_fp4 v[116:117], v79, 1.0
	v_cvt_scalef32_pk_f32_fp4 v[118:119], v79, 1.0 op_sel:[1,0,0]
	v_cvt_scalef32_pk_f32_fp4 v[120:121], v79, 1.0 op_sel:[0,1,0]
	v_cvt_scalef32_pk_f32_fp4 v[122:123], v79, 1.0 op_sel:[1,1,0]
	v_pk_fma_f32 v[28:29], v[116:117], v[102:103], v[28:29] op_sel_hi:[1,0,1]
	v_pk_fma_f32 v[60:61], v[116:117], v[110:111], v[60:61] op_sel_hi:[1,0,1]
	v_pk_fma_f32 v[30:31], v[118:119], v[102:103], v[30:31] op_sel_hi:[1,0,1]
	v_pk_fma_f32 v[62:63], v[118:119], v[110:111], v[62:63] op_sel_hi:[1,0,1]
	v_pk_fma_f32 v[32:33], v[120:121], v[102:103], v[32:33] op_sel_hi:[1,0,1]
	v_pk_fma_f32 v[64:65], v[120:121], v[110:111], v[64:65] op_sel_hi:[1,0,1]
	v_pk_fma_f32 v[34:35], v[122:123], v[102:103], v[34:35] op_sel_hi:[1,0,1]
	v_pk_fma_f32 v[66:67], v[122:123], v[110:111], v[66:67] op_sel_hi:[1,0,1]
	s_waitcnt vmcnt(4)
	v_cvt_scalef32_pk_f32_fp4 v[116:117], v80, 1.0
	v_cvt_scalef32_pk_f32_fp4 v[118:119], v80, 1.0 op_sel:[1,0,0]
	v_cvt_scalef32_pk_f32_fp4 v[120:121], v80, 1.0 op_sel:[0,1,0]
	v_cvt_scalef32_pk_f32_fp4 v[122:123], v80, 1.0 op_sel:[1,1,0]
	v_pk_fma_f32 v[4:5], v[116:117], v[102:103], v[4:5] op_sel:[0,1,0] op_sel_hi:[1,1,1]
	v_pk_fma_f32 v[36:37], v[116:117], v[110:111], v[36:37] op_sel:[0,1,0] op_sel_hi:[1,1,1]
	v_pk_fma_f32 v[6:7], v[118:119], v[102:103], v[6:7] op_sel:[0,1,0] op_sel_hi:[1,1,1]
	v_pk_fma_f32 v[38:39], v[118:119], v[110:111], v[38:39] op_sel:[0,1,0] op_sel_hi:[1,1,1]
	v_pk_fma_f32 v[8:9], v[120:121], v[102:103], v[8:9] op_sel:[0,1,0] op_sel_hi:[1,1,1]
	v_pk_fma_f32 v[40:41], v[120:121], v[110:111], v[40:41] op_sel:[0,1,0] op_sel_hi:[1,1,1]
	v_pk_fma_f32 v[10:11], v[122:123], v[102:103], v[10:11] op_sel:[0,1,0] op_sel_hi:[1,1,1]
	v_pk_fma_f32 v[42:43], v[122:123], v[110:111], v[42:43] op_sel:[0,1,0] op_sel_hi:[1,1,1]
	v_cvt_scalef32_pk_f32_fp4 v[116:117], v81, 1.0
	v_cvt_scalef32_pk_f32_fp4 v[118:119], v81, 1.0 op_sel:[1,0,0]
	v_cvt_scalef32_pk_f32_fp4 v[120:121], v81, 1.0 op_sel:[0,1,0]
	v_cvt_scalef32_pk_f32_fp4 v[122:123], v81, 1.0 op_sel:[1,1,0]
	v_pk_fma_f32 v[12:13], v[116:117], v[102:103], v[12:13] op_sel:[0,1,0] op_sel_hi:[1,1,1]
	v_pk_fma_f32 v[44:45], v[116:117], v[110:111], v[44:45] op_sel:[0,1,0] op_sel_hi:[1,1,1]
	v_pk_fma_f32 v[14:15], v[118:119], v[102:103], v[14:15] op_sel:[0,1,0] op_sel_hi:[1,1,1]
	v_pk_fma_f32 v[46:47], v[118:119], v[110:111], v[46:47] op_sel:[0,1,0] op_sel_hi:[1,1,1]
	v_pk_fma_f32 v[16:17], v[120:121], v[102:103], v[16:17] op_sel:[0,1,0] op_sel_hi:[1,1,1]
	v_pk_fma_f32 v[48:49], v[120:121], v[110:111], v[48:49] op_sel:[0,1,0] op_sel_hi:[1,1,1]
	v_pk_fma_f32 v[18:19], v[122:123], v[102:103], v[18:19] op_sel:[0,1,0] op_sel_hi:[1,1,1]
	v_pk_fma_f32 v[50:51], v[122:123], v[110:111], v[50:51] op_sel:[0,1,0] op_sel_hi:[1,1,1]
	v_cvt_scalef32_pk_f32_fp4 v[116:117], v82, 1.0
	v_cvt_scalef32_pk_f32_fp4 v[118:119], v82, 1.0 op_sel:[1,0,0]
	v_cvt_scalef32_pk_f32_fp4 v[120:121], v82, 1.0 op_sel:[0,1,0]
	v_cvt_scalef32_pk_f32_fp4 v[122:123], v82, 1.0 op_sel:[1,1,0]
	v_pk_fma_f32 v[20:21], v[116:117], v[102:103], v[20:21] op_sel:[0,1,0] op_sel_hi:[1,1,1]
	v_pk_fma_f32 v[52:53], v[116:117], v[110:111], v[52:53] op_sel:[0,1,0] op_sel_hi:[1,1,1]
	v_pk_fma_f32 v[22:23], v[118:119], v[102:103], v[22:23] op_sel:[0,1,0] op_sel_hi:[1,1,1]
	v_pk_fma_f32 v[54:55], v[118:119], v[110:111], v[54:55] op_sel:[0,1,0] op_sel_hi:[1,1,1]
	v_pk_fma_f32 v[24:25], v[120:121], v[102:103], v[24:25] op_sel:[0,1,0] op_sel_hi:[1,1,1]
	v_pk_fma_f32 v[56:57], v[120:121], v[110:111], v[56:57] op_sel:[0,1,0] op_sel_hi:[1,1,1]
	v_pk_fma_f32 v[26:27], v[122:123], v[102:103], v[26:27] op_sel:[0,1,0] op_sel_hi:[1,1,1]
	v_pk_fma_f32 v[58:59], v[122:123], v[110:111], v[58:59] op_sel:[0,1,0] op_sel_hi:[1,1,1]
	v_cvt_scalef32_pk_f32_fp4 v[116:117], v83, 1.0
	v_cvt_scalef32_pk_f32_fp4 v[118:119], v83, 1.0 op_sel:[1,0,0]
	v_cvt_scalef32_pk_f32_fp4 v[120:121], v83, 1.0 op_sel:[0,1,0]
	v_cvt_scalef32_pk_f32_fp4 v[122:123], v83, 1.0 op_sel:[1,1,0]
	v_pk_fma_f32 v[28:29], v[116:117], v[102:103], v[28:29] op_sel:[0,1,0] op_sel_hi:[1,1,1]
	v_pk_fma_f32 v[60:61], v[116:117], v[110:111], v[60:61] op_sel:[0,1,0] op_sel_hi:[1,1,1]
	v_pk_fma_f32 v[30:31], v[118:119], v[102:103], v[30:31] op_sel:[0,1,0] op_sel_hi:[1,1,1]
	v_pk_fma_f32 v[62:63], v[118:119], v[110:111], v[62:63] op_sel:[0,1,0] op_sel_hi:[1,1,1]
	v_pk_fma_f32 v[32:33], v[120:121], v[102:103], v[32:33] op_sel:[0,1,0] op_sel_hi:[1,1,1]
	v_pk_fma_f32 v[64:65], v[120:121], v[110:111], v[64:65] op_sel:[0,1,0] op_sel_hi:[1,1,1]
	v_pk_fma_f32 v[34:35], v[122:123], v[102:103], v[34:35] op_sel:[0,1,0] op_sel_hi:[1,1,1]
	v_pk_fma_f32 v[66:67], v[122:123], v[110:111], v[66:67] op_sel:[0,1,0] op_sel_hi:[1,1,1]
	s_waitcnt vmcnt(3)
	v_cvt_scalef32_pk_f32_fp4 v[116:117], v84, 1.0
	v_cvt_scalef32_pk_f32_fp4 v[118:119], v84, 1.0 op_sel:[1,0,0]
	v_cvt_scalef32_pk_f32_fp4 v[120:121], v84, 1.0 op_sel:[0,1,0]
	v_cvt_scalef32_pk_f32_fp4 v[122:123], v84, 1.0 op_sel:[1,1,0]
	v_pk_fma_f32 v[4:5], v[116:117], v[104:105], v[4:5] op_sel_hi:[1,0,1]
	v_pk_fma_f32 v[36:37], v[116:117], v[112:113], v[36:37] op_sel_hi:[1,0,1]
	v_pk_fma_f32 v[6:7], v[118:119], v[104:105], v[6:7] op_sel_hi:[1,0,1]
	v_pk_fma_f32 v[38:39], v[118:119], v[112:113], v[38:39] op_sel_hi:[1,0,1]
	v_pk_fma_f32 v[8:9], v[120:121], v[104:105], v[8:9] op_sel_hi:[1,0,1]
	v_pk_fma_f32 v[40:41], v[120:121], v[112:113], v[40:41] op_sel_hi:[1,0,1]
	v_pk_fma_f32 v[10:11], v[122:123], v[104:105], v[10:11] op_sel_hi:[1,0,1]
	v_pk_fma_f32 v[42:43], v[122:123], v[112:113], v[42:43] op_sel_hi:[1,0,1]
	v_cvt_scalef32_pk_f32_fp4 v[116:117], v85, 1.0
	v_cvt_scalef32_pk_f32_fp4 v[118:119], v85, 1.0 op_sel:[1,0,0]
	v_cvt_scalef32_pk_f32_fp4 v[120:121], v85, 1.0 op_sel:[0,1,0]
	v_cvt_scalef32_pk_f32_fp4 v[122:123], v85, 1.0 op_sel:[1,1,0]
	v_pk_fma_f32 v[12:13], v[116:117], v[104:105], v[12:13] op_sel_hi:[1,0,1]
	v_pk_fma_f32 v[44:45], v[116:117], v[112:113], v[44:45] op_sel_hi:[1,0,1]
	v_pk_fma_f32 v[14:15], v[118:119], v[104:105], v[14:15] op_sel_hi:[1,0,1]
	v_pk_fma_f32 v[46:47], v[118:119], v[112:113], v[46:47] op_sel_hi:[1,0,1]
	v_pk_fma_f32 v[16:17], v[120:121], v[104:105], v[16:17] op_sel_hi:[1,0,1]
	v_pk_fma_f32 v[48:49], v[120:121], v[112:113], v[48:49] op_sel_hi:[1,0,1]
	v_pk_fma_f32 v[18:19], v[122:123], v[104:105], v[18:19] op_sel_hi:[1,0,1]
	v_pk_fma_f32 v[50:51], v[122:123], v[112:113], v[50:51] op_sel_hi:[1,0,1]
	v_cvt_scalef32_pk_f32_fp4 v[116:117], v86, 1.0
	v_cvt_scalef32_pk_f32_fp4 v[118:119], v86, 1.0 op_sel:[1,0,0]
	v_cvt_scalef32_pk_f32_fp4 v[120:121], v86, 1.0 op_sel:[0,1,0]
	v_cvt_scalef32_pk_f32_fp4 v[122:123], v86, 1.0 op_sel:[1,1,0]
	v_pk_fma_f32 v[20:21], v[116:117], v[104:105], v[20:21] op_sel_hi:[1,0,1]
	v_pk_fma_f32 v[52:53], v[116:117], v[112:113], v[52:53] op_sel_hi:[1,0,1]
	v_pk_fma_f32 v[22:23], v[118:119], v[104:105], v[22:23] op_sel_hi:[1,0,1]
	v_pk_fma_f32 v[54:55], v[118:119], v[112:113], v[54:55] op_sel_hi:[1,0,1]
	v_pk_fma_f32 v[24:25], v[120:121], v[104:105], v[24:25] op_sel_hi:[1,0,1]
	v_pk_fma_f32 v[56:57], v[120:121], v[112:113], v[56:57] op_sel_hi:[1,0,1]
	v_pk_fma_f32 v[26:27], v[122:123], v[104:105], v[26:27] op_sel_hi:[1,0,1]
	v_pk_fma_f32 v[58:59], v[122:123], v[112:113], v[58:59] op_sel_hi:[1,0,1]
	v_cvt_scalef32_pk_f32_fp4 v[116:117], v87, 1.0
	v_cvt_scalef32_pk_f32_fp4 v[118:119], v87, 1.0 op_sel:[1,0,0]
	v_cvt_scalef32_pk_f32_fp4 v[120:121], v87, 1.0 op_sel:[0,1,0]
	v_cvt_scalef32_pk_f32_fp4 v[122:123], v87, 1.0 op_sel:[1,1,0]
	v_pk_fma_f32 v[28:29], v[116:117], v[104:105], v[28:29] op_sel_hi:[1,0,1]
	v_pk_fma_f32 v[60:61], v[116:117], v[112:113], v[60:61] op_sel_hi:[1,0,1]
	v_pk_fma_f32 v[30:31], v[118:119], v[104:105], v[30:31] op_sel_hi:[1,0,1]
	v_pk_fma_f32 v[62:63], v[118:119], v[112:113], v[62:63] op_sel_hi:[1,0,1]
	v_pk_fma_f32 v[32:33], v[120:121], v[104:105], v[32:33] op_sel_hi:[1,0,1]
	v_pk_fma_f32 v[64:65], v[120:121], v[112:113], v[64:65] op_sel_hi:[1,0,1]
	v_pk_fma_f32 v[34:35], v[122:123], v[104:105], v[34:35] op_sel_hi:[1,0,1]
	v_pk_fma_f32 v[66:67], v[122:123], v[112:113], v[66:67] op_sel_hi:[1,0,1]
	s_waitcnt vmcnt(2)
	v_cvt_scalef32_pk_f32_fp4 v[116:117], v88, 1.0
	v_cvt_scalef32_pk_f32_fp4 v[118:119], v88, 1.0 op_sel:[1,0,0]
	v_cvt_scalef32_pk_f32_fp4 v[120:121], v88, 1.0 op_sel:[0,1,0]
	v_cvt_scalef32_pk_f32_fp4 v[122:123], v88, 1.0 op_sel:[1,1,0]
	v_pk_fma_f32 v[4:5], v[116:117], v[104:105], v[4:5] op_sel:[0,1,0] op_sel_hi:[1,1,1]
	v_pk_fma_f32 v[36:37], v[116:117], v[112:113], v[36:37] op_sel:[0,1,0] op_sel_hi:[1,1,1]
	v_pk_fma_f32 v[6:7], v[118:119], v[104:105], v[6:7] op_sel:[0,1,0] op_sel_hi:[1,1,1]
	v_pk_fma_f32 v[38:39], v[118:119], v[112:113], v[38:39] op_sel:[0,1,0] op_sel_hi:[1,1,1]
	v_pk_fma_f32 v[8:9], v[120:121], v[104:105], v[8:9] op_sel:[0,1,0] op_sel_hi:[1,1,1]
	v_pk_fma_f32 v[40:41], v[120:121], v[112:113], v[40:41] op_sel:[0,1,0] op_sel_hi:[1,1,1]
	v_pk_fma_f32 v[10:11], v[122:123], v[104:105], v[10:11] op_sel:[0,1,0] op_sel_hi:[1,1,1]
	v_pk_fma_f32 v[42:43], v[122:123], v[112:113], v[42:43] op_sel:[0,1,0] op_sel_hi:[1,1,1]
	v_cvt_scalef32_pk_f32_fp4 v[116:117], v89, 1.0
	v_cvt_scalef32_pk_f32_fp4 v[118:119], v89, 1.0 op_sel:[1,0,0]
	v_cvt_scalef32_pk_f32_fp4 v[120:121], v89, 1.0 op_sel:[0,1,0]
	v_cvt_scalef32_pk_f32_fp4 v[122:123], v89, 1.0 op_sel:[1,1,0]
	v_pk_fma_f32 v[12:13], v[116:117], v[104:105], v[12:13] op_sel:[0,1,0] op_sel_hi:[1,1,1]
	v_pk_fma_f32 v[44:45], v[116:117], v[112:113], v[44:45] op_sel:[0,1,0] op_sel_hi:[1,1,1]
	v_pk_fma_f32 v[14:15], v[118:119], v[104:105], v[14:15] op_sel:[0,1,0] op_sel_hi:[1,1,1]
	v_pk_fma_f32 v[46:47], v[118:119], v[112:113], v[46:47] op_sel:[0,1,0] op_sel_hi:[1,1,1]
	v_pk_fma_f32 v[16:17], v[120:121], v[104:105], v[16:17] op_sel:[0,1,0] op_sel_hi:[1,1,1]
	v_pk_fma_f32 v[48:49], v[120:121], v[112:113], v[48:49] op_sel:[0,1,0] op_sel_hi:[1,1,1]
	v_pk_fma_f32 v[18:19], v[122:123], v[104:105], v[18:19] op_sel:[0,1,0] op_sel_hi:[1,1,1]
	v_pk_fma_f32 v[50:51], v[122:123], v[112:113], v[50:51] op_sel:[0,1,0] op_sel_hi:[1,1,1]
	v_cvt_scalef32_pk_f32_fp4 v[116:117], v90, 1.0
	v_cvt_scalef32_pk_f32_fp4 v[118:119], v90, 1.0 op_sel:[1,0,0]
	v_cvt_scalef32_pk_f32_fp4 v[120:121], v90, 1.0 op_sel:[0,1,0]
	v_cvt_scalef32_pk_f32_fp4 v[122:123], v90, 1.0 op_sel:[1,1,0]
	v_pk_fma_f32 v[20:21], v[116:117], v[104:105], v[20:21] op_sel:[0,1,0] op_sel_hi:[1,1,1]
	v_pk_fma_f32 v[52:53], v[116:117], v[112:113], v[52:53] op_sel:[0,1,0] op_sel_hi:[1,1,1]
	v_pk_fma_f32 v[22:23], v[118:119], v[104:105], v[22:23] op_sel:[0,1,0] op_sel_hi:[1,1,1]
	v_pk_fma_f32 v[54:55], v[118:119], v[112:113], v[54:55] op_sel:[0,1,0] op_sel_hi:[1,1,1]
	v_pk_fma_f32 v[24:25], v[120:121], v[104:105], v[24:25] op_sel:[0,1,0] op_sel_hi:[1,1,1]
	v_pk_fma_f32 v[56:57], v[120:121], v[112:113], v[56:57] op_sel:[0,1,0] op_sel_hi:[1,1,1]
	v_pk_fma_f32 v[26:27], v[122:123], v[104:105], v[26:27] op_sel:[0,1,0] op_sel_hi:[1,1,1]
	v_pk_fma_f32 v[58:59], v[122:123], v[112:113], v[58:59] op_sel:[0,1,0] op_sel_hi:[1,1,1]
	v_cvt_scalef32_pk_f32_fp4 v[116:117], v91, 1.0
	v_cvt_scalef32_pk_f32_fp4 v[118:119], v91, 1.0 op_sel:[1,0,0]
	v_cvt_scalef32_pk_f32_fp4 v[120:121], v91, 1.0 op_sel:[0,1,0]
	v_cvt_scalef32_pk_f32_fp4 v[122:123], v91, 1.0 op_sel:[1,1,0]
	v_pk_fma_f32 v[28:29], v[116:117], v[104:105], v[28:29] op_sel:[0,1,0] op_sel_hi:[1,1,1]
	v_pk_fma_f32 v[60:61], v[116:117], v[112:113], v[60:61] op_sel:[0,1,0] op_sel_hi:[1,1,1]
	v_pk_fma_f32 v[30:31], v[118:119], v[104:105], v[30:31] op_sel:[0,1,0] op_sel_hi:[1,1,1]
	v_pk_fma_f32 v[62:63], v[118:119], v[112:113], v[62:63] op_sel:[0,1,0] op_sel_hi:[1,1,1]
	v_pk_fma_f32 v[32:33], v[120:121], v[104:105], v[32:33] op_sel:[0,1,0] op_sel_hi:[1,1,1]
	v_pk_fma_f32 v[64:65], v[120:121], v[112:113], v[64:65] op_sel:[0,1,0] op_sel_hi:[1,1,1]
	v_pk_fma_f32 v[34:35], v[122:123], v[104:105], v[34:35] op_sel:[0,1,0] op_sel_hi:[1,1,1]
	v_pk_fma_f32 v[66:67], v[122:123], v[112:113], v[66:67] op_sel:[0,1,0] op_sel_hi:[1,1,1]
	s_waitcnt vmcnt(1)
	v_cvt_scalef32_pk_f32_fp4 v[116:117], v92, 1.0
	v_cvt_scalef32_pk_f32_fp4 v[118:119], v92, 1.0 op_sel:[1,0,0]
	v_cvt_scalef32_pk_f32_fp4 v[120:121], v92, 1.0 op_sel:[0,1,0]
	v_cvt_scalef32_pk_f32_fp4 v[122:123], v92, 1.0 op_sel:[1,1,0]
	v_pk_fma_f32 v[4:5], v[116:117], v[106:107], v[4:5] op_sel_hi:[1,0,1]
	v_pk_fma_f32 v[36:37], v[116:117], v[114:115], v[36:37] op_sel_hi:[1,0,1]
	v_pk_fma_f32 v[6:7], v[118:119], v[106:107], v[6:7] op_sel_hi:[1,0,1]
	v_pk_fma_f32 v[38:39], v[118:119], v[114:115], v[38:39] op_sel_hi:[1,0,1]
	v_pk_fma_f32 v[8:9], v[120:121], v[106:107], v[8:9] op_sel_hi:[1,0,1]
	v_pk_fma_f32 v[40:41], v[120:121], v[114:115], v[40:41] op_sel_hi:[1,0,1]
	v_pk_fma_f32 v[10:11], v[122:123], v[106:107], v[10:11] op_sel_hi:[1,0,1]
	v_pk_fma_f32 v[42:43], v[122:123], v[114:115], v[42:43] op_sel_hi:[1,0,1]
	v_cvt_scalef32_pk_f32_fp4 v[116:117], v93, 1.0
	v_cvt_scalef32_pk_f32_fp4 v[118:119], v93, 1.0 op_sel:[1,0,0]
	v_cvt_scalef32_pk_f32_fp4 v[120:121], v93, 1.0 op_sel:[0,1,0]
	v_cvt_scalef32_pk_f32_fp4 v[122:123], v93, 1.0 op_sel:[1,1,0]
	v_pk_fma_f32 v[12:13], v[116:117], v[106:107], v[12:13] op_sel_hi:[1,0,1]
	v_pk_fma_f32 v[44:45], v[116:117], v[114:115], v[44:45] op_sel_hi:[1,0,1]
	v_pk_fma_f32 v[14:15], v[118:119], v[106:107], v[14:15] op_sel_hi:[1,0,1]
	v_pk_fma_f32 v[46:47], v[118:119], v[114:115], v[46:47] op_sel_hi:[1,0,1]
	v_pk_fma_f32 v[16:17], v[120:121], v[106:107], v[16:17] op_sel_hi:[1,0,1]
	v_pk_fma_f32 v[48:49], v[120:121], v[114:115], v[48:49] op_sel_hi:[1,0,1]
	v_pk_fma_f32 v[18:19], v[122:123], v[106:107], v[18:19] op_sel_hi:[1,0,1]
	v_pk_fma_f32 v[50:51], v[122:123], v[114:115], v[50:51] op_sel_hi:[1,0,1]
	v_cvt_scalef32_pk_f32_fp4 v[116:117], v94, 1.0
	v_cvt_scalef32_pk_f32_fp4 v[118:119], v94, 1.0 op_sel:[1,0,0]
	v_cvt_scalef32_pk_f32_fp4 v[120:121], v94, 1.0 op_sel:[0,1,0]
	v_cvt_scalef32_pk_f32_fp4 v[122:123], v94, 1.0 op_sel:[1,1,0]
	v_pk_fma_f32 v[20:21], v[116:117], v[106:107], v[20:21] op_sel_hi:[1,0,1]
	v_pk_fma_f32 v[52:53], v[116:117], v[114:115], v[52:53] op_sel_hi:[1,0,1]
	v_pk_fma_f32 v[22:23], v[118:119], v[106:107], v[22:23] op_sel_hi:[1,0,1]
	v_pk_fma_f32 v[54:55], v[118:119], v[114:115], v[54:55] op_sel_hi:[1,0,1]
	v_pk_fma_f32 v[24:25], v[120:121], v[106:107], v[24:25] op_sel_hi:[1,0,1]
	v_pk_fma_f32 v[56:57], v[120:121], v[114:115], v[56:57] op_sel_hi:[1,0,1]
	v_pk_fma_f32 v[26:27], v[122:123], v[106:107], v[26:27] op_sel_hi:[1,0,1]
	v_pk_fma_f32 v[58:59], v[122:123], v[114:115], v[58:59] op_sel_hi:[1,0,1]
	v_cvt_scalef32_pk_f32_fp4 v[116:117], v95, 1.0
	v_cvt_scalef32_pk_f32_fp4 v[118:119], v95, 1.0 op_sel:[1,0,0]
	v_cvt_scalef32_pk_f32_fp4 v[120:121], v95, 1.0 op_sel:[0,1,0]
	v_cvt_scalef32_pk_f32_fp4 v[122:123], v95, 1.0 op_sel:[1,1,0]
	v_pk_fma_f32 v[28:29], v[116:117], v[106:107], v[28:29] op_sel_hi:[1,0,1]
	v_pk_fma_f32 v[60:61], v[116:117], v[114:115], v[60:61] op_sel_hi:[1,0,1]
	v_pk_fma_f32 v[30:31], v[118:119], v[106:107], v[30:31] op_sel_hi:[1,0,1]
	v_pk_fma_f32 v[62:63], v[118:119], v[114:115], v[62:63] op_sel_hi:[1,0,1]
	v_pk_fma_f32 v[32:33], v[120:121], v[106:107], v[32:33] op_sel_hi:[1,0,1]
	v_pk_fma_f32 v[64:65], v[120:121], v[114:115], v[64:65] op_sel_hi:[1,0,1]
	v_pk_fma_f32 v[34:35], v[122:123], v[106:107], v[34:35] op_sel_hi:[1,0,1]
	v_pk_fma_f32 v[66:67], v[122:123], v[114:115], v[66:67] op_sel_hi:[1,0,1]
	s_waitcnt vmcnt(0)
	v_cvt_scalef32_pk_f32_fp4 v[116:117], v96, 1.0
	v_cvt_scalef32_pk_f32_fp4 v[118:119], v96, 1.0 op_sel:[1,0,0]
	v_cvt_scalef32_pk_f32_fp4 v[120:121], v96, 1.0 op_sel:[0,1,0]
	v_cvt_scalef32_pk_f32_fp4 v[122:123], v96, 1.0 op_sel:[1,1,0]
	v_pk_fma_f32 v[4:5], v[116:117], v[106:107], v[4:5] op_sel:[0,1,0] op_sel_hi:[1,1,1]
	v_pk_fma_f32 v[36:37], v[116:117], v[114:115], v[36:37] op_sel:[0,1,0] op_sel_hi:[1,1,1]
	v_pk_fma_f32 v[6:7], v[118:119], v[106:107], v[6:7] op_sel:[0,1,0] op_sel_hi:[1,1,1]
	v_pk_fma_f32 v[38:39], v[118:119], v[114:115], v[38:39] op_sel:[0,1,0] op_sel_hi:[1,1,1]
	v_pk_fma_f32 v[8:9], v[120:121], v[106:107], v[8:9] op_sel:[0,1,0] op_sel_hi:[1,1,1]
	v_pk_fma_f32 v[40:41], v[120:121], v[114:115], v[40:41] op_sel:[0,1,0] op_sel_hi:[1,1,1]
	v_pk_fma_f32 v[10:11], v[122:123], v[106:107], v[10:11] op_sel:[0,1,0] op_sel_hi:[1,1,1]
	v_pk_fma_f32 v[42:43], v[122:123], v[114:115], v[42:43] op_sel:[0,1,0] op_sel_hi:[1,1,1]
	v_cvt_scalef32_pk_f32_fp4 v[116:117], v97, 1.0
	v_cvt_scalef32_pk_f32_fp4 v[118:119], v97, 1.0 op_sel:[1,0,0]
	v_cvt_scalef32_pk_f32_fp4 v[120:121], v97, 1.0 op_sel:[0,1,0]
	v_cvt_scalef32_pk_f32_fp4 v[122:123], v97, 1.0 op_sel:[1,1,0]
	v_pk_fma_f32 v[12:13], v[116:117], v[106:107], v[12:13] op_sel:[0,1,0] op_sel_hi:[1,1,1]
	v_pk_fma_f32 v[44:45], v[116:117], v[114:115], v[44:45] op_sel:[0,1,0] op_sel_hi:[1,1,1]
	v_pk_fma_f32 v[14:15], v[118:119], v[106:107], v[14:15] op_sel:[0,1,0] op_sel_hi:[1,1,1]
	v_pk_fma_f32 v[46:47], v[118:119], v[114:115], v[46:47] op_sel:[0,1,0] op_sel_hi:[1,1,1]
	v_pk_fma_f32 v[16:17], v[120:121], v[106:107], v[16:17] op_sel:[0,1,0] op_sel_hi:[1,1,1]
	v_pk_fma_f32 v[48:49], v[120:121], v[114:115], v[48:49] op_sel:[0,1,0] op_sel_hi:[1,1,1]
	v_pk_fma_f32 v[18:19], v[122:123], v[106:107], v[18:19] op_sel:[0,1,0] op_sel_hi:[1,1,1]
	v_pk_fma_f32 v[50:51], v[122:123], v[114:115], v[50:51] op_sel:[0,1,0] op_sel_hi:[1,1,1]
	v_cvt_scalef32_pk_f32_fp4 v[116:117], v98, 1.0
	v_cvt_scalef32_pk_f32_fp4 v[118:119], v98, 1.0 op_sel:[1,0,0]
	v_cvt_scalef32_pk_f32_fp4 v[120:121], v98, 1.0 op_sel:[0,1,0]
	v_cvt_scalef32_pk_f32_fp4 v[122:123], v98, 1.0 op_sel:[1,1,0]
	v_pk_fma_f32 v[20:21], v[116:117], v[106:107], v[20:21] op_sel:[0,1,0] op_sel_hi:[1,1,1]
	v_pk_fma_f32 v[52:53], v[116:117], v[114:115], v[52:53] op_sel:[0,1,0] op_sel_hi:[1,1,1]
	v_pk_fma_f32 v[22:23], v[118:119], v[106:107], v[22:23] op_sel:[0,1,0] op_sel_hi:[1,1,1]
	v_pk_fma_f32 v[54:55], v[118:119], v[114:115], v[54:55] op_sel:[0,1,0] op_sel_hi:[1,1,1]
	v_pk_fma_f32 v[24:25], v[120:121], v[106:107], v[24:25] op_sel:[0,1,0] op_sel_hi:[1,1,1]
	v_pk_fma_f32 v[56:57], v[120:121], v[114:115], v[56:57] op_sel:[0,1,0] op_sel_hi:[1,1,1]
	v_pk_fma_f32 v[26:27], v[122:123], v[106:107], v[26:27] op_sel:[0,1,0] op_sel_hi:[1,1,1]
	v_pk_fma_f32 v[58:59], v[122:123], v[114:115], v[58:59] op_sel:[0,1,0] op_sel_hi:[1,1,1]
	v_cvt_scalef32_pk_f32_fp4 v[116:117], v99, 1.0
	v_cvt_scalef32_pk_f32_fp4 v[118:119], v99, 1.0 op_sel:[1,0,0]
	v_cvt_scalef32_pk_f32_fp4 v[120:121], v99, 1.0 op_sel:[0,1,0]
	v_cvt_scalef32_pk_f32_fp4 v[122:123], v99, 1.0 op_sel:[1,1,0]
	v_pk_fma_f32 v[28:29], v[116:117], v[106:107], v[28:29] op_sel:[0,1,0] op_sel_hi:[1,1,1]
	v_pk_fma_f32 v[60:61], v[116:117], v[114:115], v[60:61] op_sel:[0,1,0] op_sel_hi:[1,1,1]
	v_pk_fma_f32 v[30:31], v[118:119], v[106:107], v[30:31] op_sel:[0,1,0] op_sel_hi:[1,1,1]
	v_pk_fma_f32 v[62:63], v[118:119], v[114:115], v[62:63] op_sel:[0,1,0] op_sel_hi:[1,1,1]
	v_pk_fma_f32 v[32:33], v[120:121], v[106:107], v[32:33] op_sel:[0,1,0] op_sel_hi:[1,1,1]
	v_pk_fma_f32 v[64:65], v[120:121], v[114:115], v[64:65] op_sel:[0,1,0] op_sel_hi:[1,1,1]
	v_pk_fma_f32 v[34:35], v[122:123], v[106:107], v[34:35] op_sel:[0,1,0] op_sel_hi:[1,1,1]
	v_pk_fma_f32 v[66:67], v[122:123], v[114:115], v[66:67] op_sel:[0,1,0] op_sel_hi:[1,1,1]
	v_cvt_scalef32_pk_fp4_f32 v68, v4, v5, s30
	v_cvt_scalef32_pk_fp4_f32 v68, v6, v7, s30 op_sel:[0,0,1,0]
	v_cvt_scalef32_pk_fp4_f32 v68, v8, v9, s30 op_sel:[0,0,0,1]
	v_cvt_scalef32_pk_fp4_f32 v68, v10, v11, s30 op_sel:[0,0,1,1]
	v_cvt_scalef32_pk_fp4_f32 v69, v12, v13, s30
	v_cvt_scalef32_pk_fp4_f32 v69, v14, v15, s30 op_sel:[0,0,1,0]
	v_cvt_scalef32_pk_fp4_f32 v69, v16, v17, s30 op_sel:[0,0,0,1]
	v_cvt_scalef32_pk_fp4_f32 v69, v18, v19, s30 op_sel:[0,0,1,1]
	v_cvt_scalef32_pk_fp4_f32 v70, v20, v21, s30
	v_cvt_scalef32_pk_fp4_f32 v70, v22, v23, s30 op_sel:[0,0,1,0]
	v_cvt_scalef32_pk_fp4_f32 v70, v24, v25, s30 op_sel:[0,0,0,1]
	v_cvt_scalef32_pk_fp4_f32 v70, v26, v27, s30 op_sel:[0,0,1,1]
	v_cvt_scalef32_pk_fp4_f32 v71, v28, v29, s30
	v_cvt_scalef32_pk_fp4_f32 v71, v30, v31, s30 op_sel:[0,0,1,0]
	v_cvt_scalef32_pk_fp4_f32 v71, v32, v33, s30 op_sel:[0,0,0,1]
	v_cvt_scalef32_pk_fp4_f32 v71, v34, v35, s30 op_sel:[0,0,1,1]
	v_cvt_scalef32_pk_fp4_f32 v72, v36, v37, s30
	v_cvt_scalef32_pk_fp4_f32 v72, v38, v39, s30 op_sel:[0,0,1,0]
	v_cvt_scalef32_pk_fp4_f32 v72, v40, v41, s30 op_sel:[0,0,0,1]
	v_cvt_scalef32_pk_fp4_f32 v72, v42, v43, s30 op_sel:[0,0,1,1]
	v_cvt_scalef32_pk_fp4_f32 v73, v44, v45, s30
	v_cvt_scalef32_pk_fp4_f32 v73, v46, v47, s30 op_sel:[0,0,1,0]
	v_cvt_scalef32_pk_fp4_f32 v73, v48, v49, s30 op_sel:[0,0,0,1]
	v_cvt_scalef32_pk_fp4_f32 v73, v50, v51, s30 op_sel:[0,0,1,1]
	v_cvt_scalef32_pk_fp4_f32 v74, v52, v53, s30
	v_cvt_scalef32_pk_fp4_f32 v74, v54, v55, s30 op_sel:[0,0,1,0]
	v_cvt_scalef32_pk_fp4_f32 v74, v56, v57, s30 op_sel:[0,0,0,1]
	v_cvt_scalef32_pk_fp4_f32 v74, v58, v59, s30 op_sel:[0,0,1,1]
	v_cvt_scalef32_pk_fp4_f32 v75, v60, v61, s30
	v_cvt_scalef32_pk_fp4_f32 v75, v62, v63, s30 op_sel:[0,0,1,0]
	v_cvt_scalef32_pk_fp4_f32 v75, v64, v65, s30 op_sel:[0,0,0,1]
	v_cvt_scalef32_pk_fp4_f32 v75, v66, v67, s30 op_sel:[0,0,1,1]
	global_store_dwordx4 v1, v[68:71], s[8:9]
	global_store_dwordx4 v1, v[72:75], s[32:33]
	s_endpgm

	.amdhsa_kernel _Z5k_mixPKhPKfPhi
		.amdhsa_group_segment_fixed_size 0
		.amdhsa_private_segment_fixed_size 0
		.amdhsa_kernarg_size 28
		.amdhsa_user_sgpr_count 2
		.amdhsa_user_sgpr_dispatch_ptr 0
		.amdhsa_user_sgpr_queue_ptr 0
		.amdhsa_user_sgpr_kernarg_segment_ptr 1
		.amdhsa_user_sgpr_dispatch_id 0
		.amdhsa_user_sgpr_kernarg_preload_length 0
		.amdhsa_user_sgpr_kernarg_preload_offset 0
		.amdhsa_user_sgpr_private_segment_size 0
		.amdhsa_uses_dynamic_stack 0
		.amdhsa_enable_private_segment 0
		.amdhsa_system_sgpr_workgroup_id_x 1
		.amdhsa_system_sgpr_workgroup_id_y 0
		.amdhsa_system_sgpr_workgroup_id_z 0
		.amdhsa_system_sgpr_workgroup_info 0
		.amdhsa_system_vgpr_workitem_id 0
		.amdhsa_next_free_vgpr 124
		.amdhsa_next_free_sgpr 34
		.amdhsa_accum_offset 124
		.amdhsa_reserve_vcc 1
		.amdhsa_float_round_mode_32 0
		.amdhsa_float_round_mode_16_64 0
		.amdhsa_float_denorm_mode_32 3
		.amdhsa_float_denorm_mode_16_64 3
		.amdhsa_dx10_clamp 1
		.amdhsa_ieee_mode 1
		.amdhsa_fp16_overflow 0
		.amdhsa_tg_split 0
		.amdhsa_exception_fp_ieee_invalid_op 0
		.amdhsa_exception_fp_denorm_src 0
		.amdhsa_exception_fp_ieee_div_zero 0
		.amdhsa_exception_fp_ieee_overflow 0
		.amdhsa_exception_fp_ieee_underflow 0
		.amdhsa_exception_fp_ieee_inexact 0
		.amdhsa_exception_int_div_zero 0
	.end_amdhsa_kernel

.Lfunc_end2:
	.size	_Z5k_mixPKhPKfPhi, .Lfunc_end2-_Z5k_mixPKhPKfPhi
	.set _Z5k_mixPKhPKfPhi.num_vgpr, 124
	.set _Z5k_mixPKhPKfPhi.num_agpr, 0
	.set _Z5k_mixPKhPKfPhi.numbered_sgpr, 34
	.set _Z5k_mixPKhPKfPhi.num_named_barrier, 0
	.set _Z5k_mixPKhPKfPhi.private_seg_size, 0
	.set _Z5k_mixPKhPKfPhi.uses_vcc, 1
	.set _Z5k_mixPKhPKfPhi.uses_flat_scratch, 0
	.set _Z5k_mixPKhPKfPhi.has_dyn_sized_stack, 0
	.set _Z5k_mixPKhPKfPhi.has_recursion, 0
	.set _Z5k_mixPKhPKfPhi.has_indirect_call, 0

amdhsa.kernels:
  - .agpr_count:     0
    .args:
      - .offset:         0
        .size:           80
        .value_kind:     by_value
    .group_segment_fixed_size: 8192
    .kernarg_segment_align: 8
    .kernarg_segment_size: 80
    .language:       OpenCL C
    .language_version:
      - 2
      - 0
    .max_flat_workgroup_size: 256
    .name:           _Z6k_prep8PrepArgs
    .private_segment_fixed_size: 0
    .sgpr_count:     35
    .sgpr_spill_count: 0
    .symbol:         _Z6k_prep8PrepArgs.kd
    .uniform_work_group_size: 1
    .uses_dynamic_stack: false
    .vgpr_count:     45
    .vgpr_spill_count: 0
    .wavefront_size: 64
  - .agpr_count:     4
    .args:
      - .actual_access:  read_only
        .address_space:  global
        .offset:         0
        .size:           8
        .value_kind:     global_buffer
      - .actual_access:  read_only
        .address_space:  global
        .offset:         8
        .size:           8
        .value_kind:     global_buffer
      - .actual_access:  read_only
        .address_space:  global
        .offset:         16
        .size:           8
        .value_kind:     global_buffer
      - .actual_access:  write_only
        .address_space:  global
        .offset:         24
        .size:           8
        .value_kind:     global_buffer
      - .actual_access:  write_only
        .address_space:  global
        .offset:         32
        .size:           8
        .value_kind:     global_buffer
    .group_segment_fixed_size: 36096
    .kernarg_segment_align: 8
    .kernarg_segment_size: 40
    .language:       OpenCL C
    .language_version:
      - 2
      - 0
    .max_flat_workgroup_size: 256
    .name:           _Z7k_gatesPKfPKtS0_PhPf
    .private_segment_fixed_size: 0
    .sgpr_count:     18
    .sgpr_spill_count: 0
    .symbol:         _Z7k_gatesPKfPKtS0_PhPf.kd
    .uniform_work_group_size: 1
    .uses_dynamic_stack: false
    .vgpr_count:     88
    .vgpr_spill_count: 0
    .wavefront_size: 64
  - .agpr_count:     0
    .args:
      - .actual_access:  read_only
        .address_space:  global
        .offset:         0
        .size:           8
        .value_kind:     global_buffer
      - .actual_access:  read_only
        .address_space:  global
        .offset:         8
        .size:           8
        .value_kind:     global_buffer
      - .actual_access:  write_only
        .address_space:  global
        .offset:         16
        .size:           8
        .value_kind:     global_buffer
      - .offset:         24
        .size:           4
        .value_kind:     by_value
    .group_segment_fixed_size: 0
    .kernarg_segment_align: 8
    .kernarg_segment_size: 28
    .language:       OpenCL C
    .language_version:
      - 2
      - 0
    .max_flat_workgroup_size: 256
    .name:           _Z5k_mixPKhPKfPhi
    .private_segment_fixed_size: 0
    .sgpr_count:     40
    .sgpr_spill_count: 0
    .symbol:         _Z5k_mixPKhPKfPhi.kd
    .uniform_work_group_size: 1
    .uses_dynamic_stack: false
    .vgpr_count:     124
    .vgpr_spill_count: 0
    .wavefront_size: 64
  - .agpr_count:     0
    .args:
      - .actual_access:  read_only
        .address_space:  global
        .offset:         0
        .size:           8
        .value_kind:     global_buffer
      - .actual_access:  read_only
        .address_space:  global
        .offset:         8
        .size:           8
        .value_kind:     global_buffer
      - .actual_access:  write_only
        .address_space:  global
        .offset:         16
        .size:           8
        .value_kind:     global_buffer
    .group_segment_fixed_size: 0
    .kernarg_segment_align: 8
    .kernarg_segment_size: 24
    .language:       OpenCL C
    .language_version:
      - 2
      - 0
    .max_flat_workgroup_size: 256
    .name:           _Z7k_finalPKfS0_Pf
    .private_segment_fixed_size: 0
    .sgpr_count:     16
    .sgpr_spill_count: 0
    .symbol:         _Z7k_finalPKfS0_Pf.kd
    .uniform_work_group_size: 1
    .uses_dynamic_stack: false
    .vgpr_count:     16
    .vgpr_spill_count: 0
    .wavefront_size: 64
  - .agpr_count:     0
    .args:
      - .offset:         0
        .size:           24
        .value_kind:     by_value
      - .offset:         24
        .size:           32
        .value_kind:     by_value
      - .offset:         56
        .size:           4
        .value_kind:     by_value
      - .offset:         60
        .size:           4
        .value_kind:     by_value
      - .offset:         64
        .size:           4
        .value_kind:     by_value
      - .offset:         68
        .size:           4
        .value_kind:     by_value
      - .offset:         72
        .size:           4
        .value_kind:     hidden_block_count_x
      - .offset:         76
        .size:           4
        .value_kind:     hidden_block_count_y
      - .offset:         80
        .size:           4
        .value_kind:     hidden_block_count_z
      - .offset:         84
        .size:           2
        .value_kind:     hidden_group_size_x
      - .offset:         86
        .size:           2
        .value_kind:     hidden_group_size_y
      - .offset:         88
        .size:           2
        .value_kind:     hidden_group_size_z
      - .offset:         90
        .size:           2
        .value_kind:     hidden_remainder_x
      - .offset:         92
        .size:           2
        .value_kind:     hidden_remainder_y
      - .offset:         94
        .size:           2
        .value_kind:     hidden_remainder_z
      - .offset:         112
        .size:           8
        .value_kind:     hidden_global_offset_x
      - .offset:         120
        .size:           8
        .value_kind:     hidden_global_offset_y
      - .offset:         128
        .size:           8
        .value_kind:     hidden_global_offset_z
      - .offset:         136
        .size:           2
        .value_kind:     hidden_grid_dims
      - .offset:         192
        .size:           4
        .value_kind:     hidden_dynamic_lds_size
    .group_segment_fixed_size: 0
    .kernarg_segment_align: 8
    .kernarg_segment_size: 328
    .language:       OpenCL C
    .language_version:
      - 2
      - 0
    .max_flat_workgroup_size: 512
    .name:           _Z6k_gemmI4Epi8ILi0ELb1ELb1EEEv4GemmT_iiii
    .private_segment_fixed_size: 0
    .sgpr_count:     92
    .sgpr_spill_count: 0
    .symbol:         _Z6k_gemmI4Epi8ILi0ELb1ELb1EEEv4GemmT_iiii.kd
    .uniform_work_group_size: 1
    .uses_dynamic_stack: false
    .vgpr_count:     248
    .vgpr_spill_count: 0
    .wavefront_size: 64
  - .agpr_count:     0
    .args:
      - .offset:         0
        .size:           24
        .value_kind:     by_value
      - .offset:         24
        .size:           32
        .value_kind:     by_value
      - .offset:         56
        .size:           4
        .value_kind:     by_value
      - .offset:         60
        .size:           4
        .value_kind:     by_value
      - .offset:         64
        .size:           4
        .value_kind:     by_value
      - .offset:         68
        .size:           4
        .value_kind:     by_value
      - .offset:         72
        .size:           4
        .value_kind:     hidden_block_count_x
      - .offset:         76
        .size:           4
        .value_kind:     hidden_block_count_y
      - .offset:         80
        .size:           4
        .value_kind:     hidden_block_count_z
      - .offset:         84
        .size:           2
        .value_kind:     hidden_group_size_x
      - .offset:         86
        .size:           2
        .value_kind:     hidden_group_size_y
      - .offset:         88
        .size:           2
        .value_kind:     hidden_group_size_z
      - .offset:         90
        .size:           2
        .value_kind:     hidden_remainder_x
      - .offset:         92
        .size:           2
        .value_kind:     hidden_remainder_y
      - .offset:         94
        .size:           2
        .value_kind:     hidden_remainder_z
      - .offset:         112
        .size:           8
        .value_kind:     hidden_global_offset_x
      - .offset:         120
        .size:           8
        .value_kind:     hidden_global_offset_y
      - .offset:         128
        .size:           8
        .value_kind:     hidden_global_offset_z
      - .offset:         136
        .size:           2
        .value_kind:     hidden_grid_dims
      - .offset:         192
        .size:           4
        .value_kind:     hidden_dynamic_lds_size
    .group_segment_fixed_size: 0
    .kernarg_segment_align: 8
    .kernarg_segment_size: 328
    .language:       OpenCL C
    .language_version:
      - 2
      - 0
    .max_flat_workgroup_size: 512
    .name:           _Z6k_gemmI4Epi8ILi1ELb1ELb1EEEv4GemmT_iiii
    .private_segment_fixed_size: 0
    .sgpr_count:     90
    .sgpr_spill_count: 0
    .symbol:         _Z6k_gemmI4Epi8ILi1ELb1ELb1EEEv4GemmT_iiii.kd
    .uniform_work_group_size: 1
    .uses_dynamic_stack: false
    .vgpr_count:     228
    .vgpr_spill_count: 0
    .wavefront_size: 64
  - .agpr_count:     0
    .args:
      - .offset:         0
        .size:           24
        .value_kind:     by_value
      - .offset:         24
        .size:           32
        .value_kind:     by_value
      - .offset:         56
        .size:           4
        .value_kind:     by_value
      - .offset:         60
        .size:           4
        .value_kind:     by_value
      - .offset:         64
        .size:           4
        .value_kind:     by_value
      - .offset:         68
        .size:           4
        .value_kind:     by_value
      - .offset:         72
        .size:           4
        .value_kind:     hidden_block_count_x
      - .offset:         76
        .size:           4
        .value_kind:     hidden_block_count_y
      - .offset:         80
        .size:           4
        .value_kind:     hidden_block_count_z
      - .offset:         84
        .size:           2
        .value_kind:     hidden_group_size_x
      - .offset:         86
        .size:           2
        .value_kind:     hidden_group_size_y
      - .offset:         88
        .size:           2
        .value_kind:     hidden_group_size_z
      - .offset:         90
        .size:           2
        .value_kind:     hidden_remainder_x
      - .offset:         92
        .size:           2
        .value_kind:     hidden_remainder_y
      - .offset:         94
        .size:           2
        .value_kind:     hidden_remainder_z
      - .offset:         112
        .size:           8
        .value_kind:     hidden_global_offset_x
      - .offset:         120
        .size:           8
        .value_kind:     hidden_global_offset_y
      - .offset:         128
        .size:           8
        .value_kind:     hidden_global_offset_z
      - .offset:         136
        .size:           2
        .value_kind:     hidden_grid_dims
      - .offset:         192
        .size:           4
        .value_kind:     hidden_dynamic_lds_size
    .group_segment_fixed_size: 0
    .kernarg_segment_align: 8
    .kernarg_segment_size: 328
    .language:       OpenCL C
    .language_version:
      - 2
      - 0
    .max_flat_workgroup_size: 512
    .name:           _Z6k_gemmI8EpiTowerEv4GemmT_iiii
    .private_segment_fixed_size: 0
    .sgpr_count:     92
    .sgpr_spill_count: 0
    .symbol:         _Z6k_gemmI8EpiTowerEv4GemmT_iiii.kd
    .uniform_work_group_size: 1
    .uses_dynamic_stack: false
    .vgpr_count:     230
    .vgpr_spill_count: 0
    .wavefront_size: 64
